# v19
# speedup vs baseline: 1.0106x; 1.0106x over previous
.LBB2_27:
	s_or_b64 exec, exec, s[16:17]
	v_lshl_add_u32 v3, v1, 2, v2
	v_add_u32_e32 v8, 0x4000, v3
	s_waitcnt lgkmcnt(10)
	ds_read2_b32 v[18:19], v8 offset0:128 offset1:132
	s_mov_b32 s5, 1
	s_waitcnt lgkmcnt(0)
	v_and_or_b32 v3, v18, 63, v4
	v_add_u32_e32 v7, 1, v18
	v_lshlrev_b32_e32 v3, 2, v3
	v_and_or_b32 v7, v7, 63, v4
	ds_bpermute_b32 v9, v3, v22
	v_lshlrev_b32_e32 v3, 2, v7
	ds_bpermute_b32 v10, v3, v22
	v_mov_b32_e32 v7, 0x186a0
	s_waitcnt lgkmcnt(1)
	v_subrev_u32_e32 v3, s6, v9
	v_min_i32_e32 v11, 0x17d, v3
	s_waitcnt lgkmcnt(0)
	v_sub_u32_e32 v44, v10, v9
	v_min_i32_e32 v9, 0x17f, v3
	v_min_i32_e32 v10, 0x17e, v3
	v_min_i32_e32 v12, 0x17c, v3
	v_lshl_add_u32 v9, v9, 2, v2
	v_lshl_add_u32 v10, v10, 2, v2
	v_lshl_add_u32 v11, v11, 2, v2
	v_lshl_add_u32 v12, v12, 2, v2
	ds_read_b32 v9, v9 offset:15360
	ds_read_b32 v10, v10 offset:15364
	ds_read_b32 v11, v11 offset:15368
	ds_read_b32 v12, v12 offset:15372
	v_cmp_lt_i32_e32 vcc, 0, v44
	s_waitcnt lgkmcnt(3)
	s_nop 0
	v_cndmask_b32_e32 v9, v7, v9, vcc
	v_cmp_lt_i32_e32 vcc, 1, v44
	v_lshl_or_b32 v13, v9, 7, v66
	v_lshlrev_b32_e32 v9, 2, v9
	s_waitcnt lgkmcnt(2)
	v_cndmask_b32_e32 v10, v7, v10, vcc
	v_cmp_lt_i32_e32 vcc, 2, v44
	v_lshl_or_b32 v14, v10, 7, v66
	v_lshlrev_b32_e32 v10, 2, v10
	s_waitcnt lgkmcnt(1)
	v_cndmask_b32_e32 v11, v7, v11, vcc
	v_cmp_lt_i32_e32 vcc, 3, v44
	v_lshl_or_b32 v15, v11, 7, v66
	v_lshlrev_b32_e32 v11, 2, v11
	s_waitcnt lgkmcnt(0)
	v_cndmask_b32_e32 v12, v7, v12, vcc
	v_lshl_or_b32 v16, v12, 7, v66
	global_load_dwordx2 v[38:39], v13, s[10:11]
	global_load_dwordx2 v[40:41], v14, s[10:11]
	global_load_dword v61, v9, s[12:13]
	global_load_dword v62, v10, s[12:13]
	global_load_dwordx2 v[32:33], v15, s[10:11]
	global_load_dwordx2 v[34:35], v16, s[10:11]
	v_lshlrev_b32_e32 v12, 2, v12
	global_load_dword v58, v11, s[12:13]
	global_load_dword v59, v12, s[12:13]
	v_xor_b32_e32 v9, 16, v5
	v_add_u32_e32 v10, 64, v4
	v_cmp_lt_i32_e32 vcc, v9, v10
	v_xor_b32_e32 v12, 32, v5
	v_add_u32_e32 v13, 1, v19
	v_cndmask_b32_e32 v9, v5, v9, vcc
	v_lshlrev_b32_e32 v11, 2, v9
	ds_bpermute_b32 v9, v11, v44
	v_cmp_lt_i32_e32 vcc, v12, v10
	v_and_or_b32 v13, v13, 63, v4
	v_lshlrev_b32_e32 v13, 2, v13
	v_cndmask_b32_e32 v5, v5, v12, vcc
	v_and_or_b32 v12, v19, 63, v4
	v_lshlrev_b32_e32 v12, 2, v12
	s_waitcnt lgkmcnt(0)
	v_max_i32_e32 v9, v44, v9
	v_lshlrev_b32_e32 v5, 2, v5
	ds_bpermute_b32 v12, v12, v22
	ds_bpermute_b32 v13, v13, v22
	ds_bpermute_b32 v10, v5, v9
	ds_read2_b32 v[20:21], v8 offset0:136 offset1:140
	s_waitcnt lgkmcnt(2)
	v_sub_u32_e32 v50, v13, v12
	s_waitcnt lgkmcnt(1)
	v_max_i32_e32 v8, v9, v10
	ds_bpermute_b32 v9, v11, v50
	v_readfirstlane_b32 s2, v8
	s_waitcnt lgkmcnt(1)
	v_and_or_b32 v8, v20, 63, v4
	v_lshlrev_b32_e32 v8, 2, v8
	v_add_u32_e32 v15, 1, v21
	s_waitcnt lgkmcnt(0)
	v_max_i32_e32 v10, v50, v9
	ds_bpermute_b32 v9, v8, v22
	v_add_u32_e32 v8, 1, v20
	v_and_or_b32 v8, v8, 63, v4
	v_lshlrev_b32_e32 v8, 2, v8
	ds_bpermute_b32 v14, v8, v22
	v_and_or_b32 v8, v21, 63, v4
	v_and_or_b32 v4, v15, 63, v4
	v_lshlrev_b32_e32 v8, 2, v8
	v_lshlrev_b32_e32 v4, 2, v4
	ds_bpermute_b32 v8, v8, v22
	ds_bpermute_b32 v15, v4, v22
	ds_bpermute_b32 v13, v5, v10
	s_waitcnt lgkmcnt(3)
	v_sub_u32_e32 v51, v14, v9
	v_subrev_u32_e32 v4, s6, v12
	ds_bpermute_b32 v12, v11, v51
	s_waitcnt lgkmcnt(2)
	v_sub_u32_e32 v52, v15, v8
	ds_bpermute_b32 v11, v11, v52
	s_waitcnt lgkmcnt(2)
	v_max_i32_e32 v10, v10, v13
	s_add_i32 s2, s2, 3
	v_readfirstlane_b32 s3, v10
	s_waitcnt lgkmcnt(1)
	v_max_i32_e32 v10, v51, v12
	s_waitcnt lgkmcnt(0)
	v_max_i32_e32 v11, v52, v11
	ds_bpermute_b32 v12, v5, v10
	ds_bpermute_b32 v5, v5, v11
	s_add_i32 s3, s3, 3
	s_ashr_i32 s2, s2, 2
	s_ashr_i32 s3, s3, 2
	s_max_i32 s4, s2, 1
	s_max_i32 s7, s3, 1
	s_waitcnt lgkmcnt(1)
	v_max_i32_e32 v10, v10, v12
	s_waitcnt lgkmcnt(0)
	v_max_i32_e32 v5, v11, v5
	s_cmp_lt_i32 s2, 2
	v_readfirstlane_b32 s16, v10
	v_readfirstlane_b32 s17, v5
	s_cselect_b64 vcc, -1, 0
	s_cmp_gt_i32 s2, 1
	s_mov_b32 s21, s4
	v_mov_b32_e32 v5, v44
	s_cbranch_scc1 .LBB2_29
	s_mov_b32 s20, 1
	s_mov_b32 s5, 0
	s_mov_b32 s21, s7
	v_mov_b32_e32 v5, v50
	v_mov_b32_e32 v3, v4
.LBB2_29:
	s_lshl_b32 s22, s5, 2
	v_add_u32_e32 v10, s22, v3
	v_min_i32_e32 v11, 0x17f, v10
	v_min_i32_e32 v12, 0x17e, v10
	v_min_i32_e32 v13, 0x17d, v10
	v_min_i32_e32 v10, 0x17c, v10
	v_lshl_add_u32 v11, v11, 2, v2
	v_lshl_add_u32 v12, v12, 2, v2
	v_lshl_add_u32 v13, v13, 2, v2
	v_lshl_add_u32 v10, v10, 2, v2
	ds_read_b32 v11, v11 offset:15360
	ds_read_b32 v12, v12 offset:15364
	ds_read_b32 v13, v13 offset:15368
	ds_read_b32 v10, v10 offset:15372
	v_cmp_lt_i32_e64 s[2:3], s22, v5
	s_add_i32 s16, s16, 3
	s_add_i32 s27, s5, 1
	s_waitcnt lgkmcnt(3)
	v_cndmask_b32_e64 v11, v7, v11, s[2:3]
	s_or_b32 s2, s22, 1
	v_cmp_lt_i32_e64 s[2:3], s2, v5
	s_waitcnt lgkmcnt(2)
	s_nop 0
	v_cndmask_b32_e64 v12, v7, v12, s[2:3]
	s_or_b32 s2, s22, 2
	v_cmp_lt_i32_e64 s[2:3], s2, v5
	v_lshl_or_b32 v14, v12, 7, v66
	s_waitcnt lgkmcnt(1)
	v_cndmask_b32_e64 v13, v7, v13, s[2:3]
	s_or_b32 s2, s22, 3
	v_cmp_lt_i32_e64 s[2:3], s2, v5
	v_lshl_or_b32 v15, v13, 7, v66
	s_waitcnt lgkmcnt(0)
	v_cndmask_b32_e64 v7, v7, v10, s[2:3]
	v_lshl_or_b32 v10, v11, 7, v66
	v_lshl_or_b32 v16, v7, 7, v66
	global_load_dwordx2 v[26:27], v10, s[10:11]
	global_load_dwordx2 v[28:29], v14, s[10:11]
	v_lshlrev_b32_e32 v10, 2, v11
	v_lshlrev_b32_e32 v11, 2, v12
	global_load_dword v56, v10, s[12:13]
	global_load_dword v57, v11, s[12:13]
	global_load_dwordx2 v[22:23], v15, s[10:11]
	global_load_dwordx2 v[24:25], v16, s[10:11]
	v_lshlrev_b32_e32 v12, 2, v13
	v_lshlrev_b32_e32 v7, 2, v7
	global_load_dword v54, v12, s[12:13]
	global_load_dword v55, v7, s[12:13]
	s_ashr_i32 s2, s16, 2
	s_max_i32 s16, s2, 1
	s_cmp_lg_u32 s27, s21
	v_subrev_u32_e32 v7, s6, v9
	s_cbranch_scc1 .LBB2_31
	s_and_b64 s[2:3], vcc, exec
	s_cselect_b32 s21, s16, s7
	v_cndmask_b32_e32 v5, v50, v51, vcc
	v_cndmask_b32_e32 v3, v4, v7, vcc
	s_add_i32 s20, s20, 1
	s_mov_b32 s27, 0

.LBB2_35:
	s_lshl_b32 s28, s27, 2
	v_add_u32_e32 v79, s28, v3
	v_lshl_add_u32 v79, v79, 2, v2
	ds_read_b32 v80, v79 offset:15360
	ds_read_b32 v81, v79 offset:15364
	ds_read_b32 v82, v79 offset:15368
	ds_read_b32 v79, v79 offset:15372
	v_cmp_lt_i32_e32 vcc, s28, v5
	s_or_b32 s29, s28, 1
	s_or_b32 s30, s28, 2
	s_waitcnt lgkmcnt(0)
	v_cndmask_b32_e32 v87, v9, v80, vcc
	v_cmp_lt_i32_e32 vcc, s29, v5
	s_or_b32 s31, s28, 3
	s_nop 0
	v_cndmask_b32_e32 v88, v9, v81, vcc
	v_cmp_lt_i32_e32 vcc, s30, v5
	v_lshl_or_b32 v83, v87, 7, v66
	v_lshlrev_b32_e32 v87, 2, v87
	v_cndmask_b32_e32 v89, v9, v82, vcc
	v_cmp_lt_i32_e32 vcc, s31, v5
	v_lshl_or_b32 v84, v88, 7, v66
	v_lshl_or_b32 v85, v89, 7, v66
	v_cndmask_b32_e32 v90, v9, v79, vcc
	v_lshl_or_b32 v86, v90, 7, v66
	v_lshlrev_b32_e32 v88, 2, v88
	v_lshlrev_b32_e32 v89, 2, v89
	v_lshlrev_b32_e32 v90, 2, v90
	s_waitcnt vmcnt(12)
	v_cvt_pk_f16_f32 v10, v61, v62
	v_perm_b32 v11, v40, v38, s23
	v_dot2c_f32_f16_e32 v60, v11, v10
	v_perm_b32 v11, v40, v38, s24
	v_dot2c_f32_f16_e32 v42, v11, v10
	v_perm_b32 v11, v40, v38, s25
	v_dot2c_f32_f16_e32 v43, v11, v10
	v_perm_b32 v11, v40, v38, s26
	v_dot2c_f32_f16_e32 v36, v11, v10
	v_perm_b32 v11, v41, v39, s23
	v_dot2c_f32_f16_e32 v37, v11, v10
	v_perm_b32 v11, v41, v39, s24
	v_dot2c_f32_f16_e32 v30, v11, v10
	v_perm_b32 v11, v41, v39, s25
	v_dot2c_f32_f16_e32 v31, v11, v10
	v_perm_b32 v11, v41, v39, s26
	v_dot2c_f32_f16_e32 v53, v11, v10
	v_dot2c_f32_f16_e32 v45, 0x3c003c00, v10
	s_waitcnt vmcnt(8)
	v_cvt_pk_f16_f32 v10, v58, v59
	v_perm_b32 v11, v34, v32, s23
	v_dot2c_f32_f16_e32 v60, v11, v10
	v_perm_b32 v11, v34, v32, s24
	v_dot2c_f32_f16_e32 v42, v11, v10
	v_perm_b32 v11, v34, v32, s25
	v_dot2c_f32_f16_e32 v43, v11, v10
	v_perm_b32 v11, v34, v32, s26
	v_dot2c_f32_f16_e32 v36, v11, v10
	v_perm_b32 v11, v35, v33, s23
	v_dot2c_f32_f16_e32 v37, v11, v10
	v_perm_b32 v11, v35, v33, s24
	v_dot2c_f32_f16_e32 v30, v11, v10
	v_perm_b32 v11, v35, v33, s25
	v_dot2c_f32_f16_e32 v31, v11, v10
	v_perm_b32 v11, v35, v33, s26
	s_add_i32 s5, s5, 1
	v_dot2c_f32_f16_e32 v53, v11, v10
	s_cmp_lg_u32 s5, s4
	v_dot2c_f32_f16_e32 v45, 0x3c003c00, v10
	s_cbranch_scc1 .LBB2_43
	v_cmp_gt_i32_e32 vcc, 15, v18
	s_and_saveexec_b64 s[4:5], vcc
	s_cbranch_execz .LBB2_38
	v_max_i32_e32 v10, 1, v44
	v_cvt_f32_u32_e32 v10, v10
	v_rcp_iflag_f32_e32 v44, v10
	s_nop 0
	v_pk_mul_f32 v[10:11], v[44:45], s[2:3]
	s_nop 0
	v_mul_f32_e32 v14, 0x4b800000, v10
	v_pk_mul_f32 v[16:17], v[10:11], v[10:11] op_sel:[0,1] op_sel_hi:[1,0]
	s_nop 0
	v_fma_mixlo_f16 v15, v60, v14, v16
	v_pk_fma_f32 v[10:11], v[42:43], v[14:15], v[16:17] op_sel_hi:[1,0,0]
	v_pk_fma_f32 v[12:13], v[36:37], v[14:15], v[16:17] op_sel_hi:[1,0,0]
	v_pk_fma_f32 v[30:31], v[30:31], v[14:15], v[16:17] op_sel_hi:[1,0,0]
	v_cvt_pk_f16_f32 v11, v10, v11
	v_cvt_pk_f16_f32 v12, v12, v13
	v_cvt_pk_f16_f32 v13, v30, v31
	v_pack_b32_f16 v10, v15, v11
	v_alignbit_b32 v11, v12, v11, 16
	v_alignbit_b32 v12, v13, v12, 16
	v_lshrrev_b32_e32 v13, 16, v13
	v_fma_mixhi_f16 v13, v53, v14, v16
	v_add_u32_e32 v14, v18, v77
	v_xor_b32_e32 v15, v14, v0
	v_lshlrev_b32_e32 v15, 4, v15
	v_and_b32_e32 v15, 0xf0, v15
	v_lshl_or_b32 v14, v14, 8, v15
	ds_write_b128 v14, v[10:13]

.LBB2_43:
	s_add_i32 s27, s27, 1
	global_load_dwordx2 v[38:39], v83, s[10:11]
	global_load_dwordx2 v[40:41], v84, s[10:11]
	global_load_dword v61, v87, s[12:13]
	global_load_dword v62, v88, s[12:13]
	global_load_dwordx2 v[32:33], v85, s[10:11]
	global_load_dwordx2 v[34:35], v86, s[10:11]
	global_load_dword v58, v89, s[12:13]
	global_load_dword v59, v90, s[12:13]
	s_cmp_lg_u32 s27, s21
	s_cbranch_scc1 .LBB2_49
	s_cmp_eq_u32 s20, 0
	s_cbranch_scc1 .LBB2_47
	s_add_i32 s27, s20, 1
	s_mov_b32 s20, 2
	s_cmp_eq_u32 s27, 2
	v_mov_b32_e32 v3, v7
	v_mov_b32_e32 v5, v51
	s_mov_b32 s21, s16
	s_cbranch_scc1 .LBB2_48
	s_cmp_eq_u32 s27, 3
	s_cselect_b64 vcc, -1, 0
	s_and_b64 s[20:21], vcc, exec
	v_cndmask_b32_e32 v5, 0, v52, vcc
	s_cselect_b32 s21, s6, 0x7fffffff
	s_mov_b32 s20, s27
	v_mov_b32_e32 v3, v8
	s_branch .LBB2_48

.LBB2_49:
	s_lshl_b32 s28, s27, 2
	v_add_u32_e32 v79, s28, v3
	v_lshl_add_u32 v79, v79, 2, v2
	ds_read_b32 v80, v79 offset:15360
	ds_read_b32 v81, v79 offset:15364
	ds_read_b32 v82, v79 offset:15368
	ds_read_b32 v79, v79 offset:15372
	v_cmp_lt_i32_e32 vcc, s28, v5
	s_or_b32 s29, s28, 1
	s_or_b32 s30, s28, 2
	s_waitcnt lgkmcnt(0)
	v_cndmask_b32_e32 v87, v9, v80, vcc
	v_cmp_lt_i32_e32 vcc, s29, v5
	s_or_b32 s31, s28, 3
	s_nop 0
	v_cndmask_b32_e32 v88, v9, v81, vcc
	v_cmp_lt_i32_e32 vcc, s30, v5
	v_lshl_or_b32 v83, v87, 7, v66
	v_lshlrev_b32_e32 v87, 2, v87
	v_cndmask_b32_e32 v89, v9, v82, vcc
	v_cmp_lt_i32_e32 vcc, s31, v5
	v_lshl_or_b32 v84, v88, 7, v66
	v_lshl_or_b32 v85, v89, 7, v66
	v_cndmask_b32_e32 v90, v9, v79, vcc
	v_lshl_or_b32 v86, v90, 7, v66
	v_lshlrev_b32_e32 v88, 2, v88
	v_lshlrev_b32_e32 v89, 2, v89
	v_lshlrev_b32_e32 v90, 2, v90
	s_waitcnt vmcnt(12)
	v_cvt_pk_f16_f32 v10, v56, v57
	v_perm_b32 v11, v28, v26, s23
	v_dot2c_f32_f16_e32 v60, v11, v10
	v_perm_b32 v11, v28, v26, s24
	v_dot2c_f32_f16_e32 v42, v11, v10
	v_perm_b32 v11, v28, v26, s25
	v_dot2c_f32_f16_e32 v43, v11, v10
	v_perm_b32 v11, v28, v26, s26
	v_dot2c_f32_f16_e32 v36, v11, v10
	v_perm_b32 v11, v29, v27, s23
	v_dot2c_f32_f16_e32 v37, v11, v10
	v_perm_b32 v11, v29, v27, s24
	v_dot2c_f32_f16_e32 v30, v11, v10
	v_perm_b32 v11, v29, v27, s25
	v_dot2c_f32_f16_e32 v31, v11, v10
	v_perm_b32 v11, v29, v27, s26
	v_dot2c_f32_f16_e32 v53, v11, v10
	v_dot2c_f32_f16_e32 v45, 0x3c003c00, v10
	s_waitcnt vmcnt(8)
	v_cvt_pk_f16_f32 v10, v54, v55
	v_perm_b32 v11, v24, v22, s23
	v_dot2c_f32_f16_e32 v60, v11, v10
	v_perm_b32 v11, v24, v22, s24
	v_dot2c_f32_f16_e32 v42, v11, v10
	v_perm_b32 v11, v24, v22, s25
	v_dot2c_f32_f16_e32 v43, v11, v10
	v_perm_b32 v11, v24, v22, s26
	v_dot2c_f32_f16_e32 v36, v11, v10
	v_perm_b32 v11, v25, v23, s23
	v_dot2c_f32_f16_e32 v37, v11, v10
	v_perm_b32 v11, v25, v23, s24
	v_dot2c_f32_f16_e32 v30, v11, v10
	v_perm_b32 v11, v25, v23, s25
	v_dot2c_f32_f16_e32 v31, v11, v10
	v_perm_b32 v11, v25, v23, s26
	s_add_i32 s5, s5, 1
	v_dot2c_f32_f16_e32 v53, v11, v10
	s_cmp_lg_u32 s5, s4
	v_dot2c_f32_f16_e32 v45, 0x3c003c00, v10
	s_cbranch_scc1 .LBB2_57
	v_cmp_gt_i32_e32 vcc, 15, v18
	s_and_saveexec_b64 s[4:5], vcc
	s_cbranch_execz .LBB2_52
	v_max_i32_e32 v10, 1, v44
	v_cvt_f32_u32_e32 v10, v10
	v_rcp_iflag_f32_e32 v44, v10
	s_nop 0
	v_pk_mul_f32 v[10:11], v[44:45], s[2:3]
	s_nop 0
	v_mul_f32_e32 v14, 0x4b800000, v10
	v_pk_mul_f32 v[16:17], v[10:11], v[10:11] op_sel:[0,1] op_sel_hi:[1,0]
	s_nop 0
	v_fma_mixlo_f16 v15, v60, v14, v16
	v_pk_fma_f32 v[10:11], v[42:43], v[14:15], v[16:17] op_sel_hi:[1,0,0]
	v_pk_fma_f32 v[12:13], v[36:37], v[14:15], v[16:17] op_sel_hi:[1,0,0]
	v_pk_fma_f32 v[22:23], v[30:31], v[14:15], v[16:17] op_sel_hi:[1,0,0]
	v_cvt_pk_f16_f32 v11, v10, v11
	v_cvt_pk_f16_f32 v12, v12, v13
	v_cvt_pk_f16_f32 v13, v22, v23
	v_pack_b32_f16 v10, v15, v11
	v_alignbit_b32 v11, v12, v11, 16
	v_alignbit_b32 v12, v13, v12, 16
	v_lshrrev_b32_e32 v13, 16, v13
	v_fma_mixhi_f16 v13, v53, v14, v16
	v_add_u32_e32 v14, v18, v77
	v_xor_b32_e32 v15, v14, v0
	v_lshlrev_b32_e32 v15, 4, v15
	v_and_b32_e32 v15, 0xf0, v15
	v_lshl_or_b32 v14, v14, 8, v15
	ds_write_b128 v14, v[10:13]

.LBB2_57:
	s_add_i32 s27, s27, 1
	global_load_dwordx2 v[26:27], v83, s[10:11]
	global_load_dwordx2 v[28:29], v84, s[10:11]
	global_load_dword v56, v87, s[12:13]
	global_load_dword v57, v88, s[12:13]
	global_load_dwordx2 v[22:23], v85, s[10:11]
	global_load_dwordx2 v[24:25], v86, s[10:11]
	global_load_dword v54, v89, s[12:13]
	global_load_dword v55, v90, s[12:13]
	s_cmp_lg_u32 s27, s21
	s_cbranch_scc1 .LBB2_34
	s_cmp_eq_u32 s20, 0
	s_cbranch_scc1 .LBB2_32
	s_add_i32 s27, s20, 1
	s_mov_b32 s20, 2
	s_cmp_eq_u32 s27, 2
	v_mov_b32_e32 v3, v7
	v_mov_b32_e32 v5, v51
	s_mov_b32 s21, s16
	s_cbranch_scc1 .LBB2_33
	s_cmp_eq_u32 s27, 3
	s_cselect_b64 vcc, -1, 0
	s_and_b64 s[20:21], vcc, exec
	v_cndmask_b32_e32 v5, 0, v52, vcc
	s_cselect_b32 s21, s6, 0x7fffffff
	s_mov_b32 s20, s27
	v_mov_b32_e32 v3, v8
	s_branch .LBB2_33

.LBB3_25:
	s_or_b64 exec, exec, s[14:15]
	v_lshl_add_u32 v3, v73, 2, v2
	v_add_u32_e32 v7, 0x4000, v3
	s_waitcnt lgkmcnt(10)
	ds_read2_b32 v[18:19], v7 offset0:128 offset1:132
	s_mov_b32 s5, 1
	s_waitcnt lgkmcnt(0)
	v_and_or_b32 v3, v18, 63, v4
	v_add_u32_e32 v6, 1, v18
	v_lshlrev_b32_e32 v3, 2, v3
	v_and_or_b32 v6, v6, 63, v4
	ds_bpermute_b32 v8, v3, v22
	v_lshlrev_b32_e32 v3, 2, v6
	ds_bpermute_b32 v9, v3, v22
	v_mov_b32_e32 v6, 0x186a0
	s_waitcnt lgkmcnt(1)
	v_subrev_u32_e32 v3, s6, v8
	v_min_i32_e32 v10, 0x17d, v3
	s_waitcnt lgkmcnt(0)
	v_sub_u32_e32 v44, v9, v8
	v_min_i32_e32 v8, 0x17f, v3
	v_min_i32_e32 v9, 0x17e, v3
	v_min_i32_e32 v11, 0x17c, v3
	v_lshl_add_u32 v8, v8, 2, v2
	v_lshl_add_u32 v9, v9, 2, v2
	v_lshl_add_u32 v10, v10, 2, v2
	v_lshl_add_u32 v11, v11, 2, v2
	ds_read_b32 v8, v8 offset:15360
	ds_read_b32 v9, v9 offset:15364
	ds_read_b32 v10, v10 offset:15368
	ds_read_b32 v11, v11 offset:15372
	v_cmp_lt_i32_e32 vcc, 0, v44
	s_waitcnt lgkmcnt(3)
	s_nop 0
	v_cndmask_b32_e32 v8, v6, v8, vcc
	v_cmp_lt_i32_e32 vcc, 1, v44
	v_lshl_or_b32 v12, v8, 7, v78
	v_lshlrev_b32_e32 v8, 2, v8
	s_waitcnt lgkmcnt(2)
	v_cndmask_b32_e32 v9, v6, v9, vcc
	v_cmp_lt_i32_e32 vcc, 2, v44
	v_lshl_or_b32 v13, v9, 7, v78
	v_lshlrev_b32_e32 v9, 2, v9
	s_waitcnt lgkmcnt(1)
	v_cndmask_b32_e32 v10, v6, v10, vcc
	v_cmp_lt_i32_e32 vcc, 3, v44
	v_lshl_or_b32 v14, v10, 7, v78
	v_lshlrev_b32_e32 v10, 2, v10
	s_waitcnt lgkmcnt(0)
	v_cndmask_b32_e32 v11, v6, v11, vcc
	v_lshl_or_b32 v15, v11, 7, v78
	global_load_dwordx2 v[38:39], v12, s[10:11]
	global_load_dwordx2 v[40:41], v13, s[10:11]
	global_load_dword v57, v8, s[12:13]
	global_load_dword v58, v9, s[12:13]
	global_load_dwordx2 v[32:33], v14, s[10:11]
	global_load_dwordx2 v[34:35], v15, s[10:11]
	v_lshlrev_b32_e32 v11, 2, v11
	global_load_dword v54, v10, s[12:13]
	global_load_dword v55, v11, s[12:13]
	v_xor_b32_e32 v8, 16, v5
	v_add_u32_e32 v9, 64, v4
	v_cmp_lt_i32_e32 vcc, v8, v9
	v_xor_b32_e32 v11, 32, v5
	v_add_u32_e32 v12, 1, v19
	v_cndmask_b32_e32 v8, v5, v8, vcc
	v_lshlrev_b32_e32 v10, 2, v8
	ds_bpermute_b32 v8, v10, v44
	v_cmp_lt_i32_e32 vcc, v11, v9
	v_and_or_b32 v12, v12, 63, v4
	v_lshlrev_b32_e32 v12, 2, v12
	v_cndmask_b32_e32 v5, v5, v11, vcc
	v_and_or_b32 v11, v19, 63, v4
	v_lshlrev_b32_e32 v11, 2, v11
	s_waitcnt lgkmcnt(0)
	v_max_i32_e32 v8, v44, v8
	v_lshlrev_b32_e32 v5, 2, v5
	ds_bpermute_b32 v11, v11, v22
	ds_bpermute_b32 v12, v12, v22
	ds_bpermute_b32 v9, v5, v8
	ds_read2_b32 v[20:21], v7 offset0:136 offset1:140
	s_waitcnt lgkmcnt(2)
	v_sub_u32_e32 v46, v12, v11
	s_waitcnt lgkmcnt(1)
	v_max_i32_e32 v7, v8, v9
	ds_bpermute_b32 v8, v10, v46
	v_readfirstlane_b32 s2, v7
	s_waitcnt lgkmcnt(1)
	v_and_or_b32 v7, v20, 63, v4
	v_lshlrev_b32_e32 v7, 2, v7
	v_add_u32_e32 v14, 1, v21
	s_waitcnt lgkmcnt(0)
	v_max_i32_e32 v9, v46, v8
	ds_bpermute_b32 v8, v7, v22
	v_add_u32_e32 v7, 1, v20
	v_and_or_b32 v7, v7, 63, v4
	v_lshlrev_b32_e32 v7, 2, v7
	ds_bpermute_b32 v13, v7, v22
	v_and_or_b32 v7, v21, 63, v4
	v_and_or_b32 v4, v14, 63, v4
	v_lshlrev_b32_e32 v7, 2, v7
	v_lshlrev_b32_e32 v4, 2, v4
	ds_bpermute_b32 v7, v7, v22
	ds_bpermute_b32 v14, v4, v22
	ds_bpermute_b32 v12, v5, v9
	s_waitcnt lgkmcnt(3)
	v_sub_u32_e32 v47, v13, v8
	v_subrev_u32_e32 v4, s6, v11
	ds_bpermute_b32 v11, v10, v47
	s_waitcnt lgkmcnt(2)
	v_sub_u32_e32 v48, v14, v7
	ds_bpermute_b32 v10, v10, v48
	s_waitcnt lgkmcnt(2)
	v_max_i32_e32 v9, v9, v12
	s_add_i32 s2, s2, 3
	v_readfirstlane_b32 s3, v9
	s_waitcnt lgkmcnt(1)
	v_max_i32_e32 v9, v47, v11
	s_waitcnt lgkmcnt(0)
	v_max_i32_e32 v10, v48, v10
	ds_bpermute_b32 v11, v5, v9
	ds_bpermute_b32 v5, v5, v10
	s_add_i32 s3, s3, 3
	s_ashr_i32 s2, s2, 2
	s_ashr_i32 s3, s3, 2
	s_max_i32 s4, s2, 1
	s_max_i32 s14, s3, 1
	s_waitcnt lgkmcnt(1)
	v_max_i32_e32 v9, v9, v11
	s_waitcnt lgkmcnt(0)
	v_max_i32_e32 v5, v10, v5
	s_cmp_lt_i32 s2, 2
	v_readfirstlane_b32 s15, v9
	v_readfirstlane_b32 s18, v5
	s_cselect_b64 vcc, -1, 0
	s_cmp_gt_i32 s2, 1
	s_mov_b32 s19, s4
	v_mov_b32_e32 v5, v44
	s_cbranch_scc1 .LBB3_27
	s_mov_b32 s7, 1
	s_mov_b32 s5, 0
	s_mov_b32 s19, s14
	v_mov_b32_e32 v5, v46
	v_mov_b32_e32 v3, v4
.LBB3_27:
	s_lshl_b32 s20, s5, 2
	v_add_u32_e32 v9, s20, v3
	v_min_i32_e32 v10, 0x17f, v9
	v_min_i32_e32 v11, 0x17e, v9
	v_min_i32_e32 v12, 0x17d, v9
	v_min_i32_e32 v9, 0x17c, v9
	v_lshl_add_u32 v10, v10, 2, v2
	v_lshl_add_u32 v11, v11, 2, v2
	v_lshl_add_u32 v12, v12, 2, v2
	v_lshl_add_u32 v9, v9, 2, v2
	ds_read_b32 v10, v10 offset:15360
	ds_read_b32 v11, v11 offset:15364
	ds_read_b32 v12, v12 offset:15368
	ds_read_b32 v9, v9 offset:15372
	v_cmp_lt_i32_e64 s[2:3], s20, v5
	s_add_i32 s15, s15, 3
	s_add_i32 s25, s5, 1
	s_waitcnt lgkmcnt(3)
	v_cndmask_b32_e64 v10, v6, v10, s[2:3]
	s_or_b32 s2, s20, 1
	v_cmp_lt_i32_e64 s[2:3], s2, v5
	s_waitcnt lgkmcnt(2)
	s_nop 0
	v_cndmask_b32_e64 v11, v6, v11, s[2:3]
	s_or_b32 s2, s20, 2
	v_cmp_lt_i32_e64 s[2:3], s2, v5
	v_lshl_or_b32 v13, v11, 7, v78
	s_waitcnt lgkmcnt(1)
	v_cndmask_b32_e64 v12, v6, v12, s[2:3]
	s_or_b32 s2, s20, 3
	v_cmp_lt_i32_e64 s[2:3], s2, v5
	v_lshl_or_b32 v14, v12, 7, v78
	s_waitcnt lgkmcnt(0)
	v_cndmask_b32_e64 v6, v6, v9, s[2:3]
	v_lshl_or_b32 v9, v10, 7, v78
	v_lshl_or_b32 v15, v6, 7, v78
	global_load_dwordx2 v[26:27], v9, s[10:11]
	global_load_dwordx2 v[28:29], v13, s[10:11]
	v_lshlrev_b32_e32 v9, 2, v10
	v_lshlrev_b32_e32 v10, 2, v11
	global_load_dword v52, v9, s[12:13]
	global_load_dword v53, v10, s[12:13]
	global_load_dwordx2 v[22:23], v14, s[10:11]
	global_load_dwordx2 v[24:25], v15, s[10:11]
	v_lshlrev_b32_e32 v11, 2, v12
	v_lshlrev_b32_e32 v6, 2, v6
	global_load_dword v50, v11, s[12:13]
	global_load_dword v51, v6, s[12:13]
	s_ashr_i32 s2, s15, 2
	s_max_i32 s15, s2, 1
	s_cmp_lg_u32 s25, s19
	v_subrev_u32_e32 v6, s6, v8
	s_cbranch_scc1 .LBB3_29
	s_and_b64 s[2:3], vcc, exec
	s_cselect_b32 s19, s15, s14
	v_cndmask_b32_e32 v5, v46, v47, vcc
	v_cndmask_b32_e32 v3, v4, v6, vcc
	s_add_i32 s7, s7, 1
	s_mov_b32 s25, 0

.LBB3_33:
	s_lshl_b32 s26, s25, 2
	v_add_u32_e32 v82, s26, v3
	v_lshl_add_u32 v82, v82, 2, v2
	ds_read_b32 v83, v82 offset:15360
	ds_read_b32 v84, v82 offset:15364
	ds_read_b32 v85, v82 offset:15368
	ds_read_b32 v82, v82 offset:15372
	v_cmp_lt_i32_e32 vcc, s26, v5
	s_or_b32 s28, s26, 1
	s_or_b32 s29, s26, 2
	s_waitcnt lgkmcnt(0)
	v_cndmask_b32_e32 v87, v8, v83, vcc
	v_cmp_lt_i32_e32 vcc, s28, v5
	s_or_b32 s30, s26, 3
	s_nop 0
	v_cndmask_b32_e32 v88, v8, v84, vcc
	v_cmp_lt_i32_e32 vcc, s29, v5
	v_lshl_or_b32 v79, v87, 7, v78
	v_lshlrev_b32_e32 v87, 2, v87
	v_cndmask_b32_e32 v89, v8, v85, vcc
	v_cmp_lt_i32_e32 vcc, s30, v5
	v_lshl_or_b32 v80, v88, 7, v78
	v_lshl_or_b32 v81, v89, 7, v78
	v_cndmask_b32_e32 v90, v8, v82, vcc
	v_lshl_or_b32 v86, v90, 7, v78
	v_lshlrev_b32_e32 v88, 2, v88
	v_lshlrev_b32_e32 v89, 2, v89
	v_lshlrev_b32_e32 v90, 2, v90
	s_waitcnt vmcnt(12)
	v_cvt_pk_f16_f32 v9, v57, v58
	v_perm_b32 v10, v40, v38, s21
	v_dot2c_f32_f16_e32 v56, v10, v9
	v_perm_b32 v10, v40, v38, s22
	v_dot2c_f32_f16_e32 v42, v10, v9
	v_perm_b32 v10, v40, v38, s23
	v_dot2c_f32_f16_e32 v43, v10, v9
	v_perm_b32 v10, v40, v38, s24
	v_dot2c_f32_f16_e32 v36, v10, v9
	v_perm_b32 v10, v41, v39, s21
	v_dot2c_f32_f16_e32 v37, v10, v9
	v_perm_b32 v10, v41, v39, s22
	v_dot2c_f32_f16_e32 v30, v10, v9
	v_perm_b32 v10, v41, v39, s23
	v_dot2c_f32_f16_e32 v31, v10, v9
	v_perm_b32 v10, v41, v39, s24
	v_dot2c_f32_f16_e32 v49, v10, v9
	s_waitcnt vmcnt(8)
	v_cvt_pk_f16_f32 v9, v54, v55
	v_perm_b32 v10, v34, v32, s21
	v_dot2c_f32_f16_e32 v56, v10, v9
	v_perm_b32 v10, v34, v32, s22
	v_dot2c_f32_f16_e32 v42, v10, v9
	v_perm_b32 v10, v34, v32, s23
	v_dot2c_f32_f16_e32 v43, v10, v9
	v_perm_b32 v10, v34, v32, s24
	v_dot2c_f32_f16_e32 v36, v10, v9
	v_perm_b32 v10, v35, v33, s21
	v_dot2c_f32_f16_e32 v37, v10, v9
	v_perm_b32 v10, v35, v33, s22
	v_dot2c_f32_f16_e32 v30, v10, v9
	v_perm_b32 v10, v35, v33, s23
	v_dot2c_f32_f16_e32 v31, v10, v9
	v_perm_b32 v10, v35, v33, s24
	s_add_i32 s5, s5, 1
	v_dot2c_f32_f16_e32 v49, v10, v9
	s_cmp_lg_u32 s5, s4
	s_cbranch_scc1 .LBB3_41
	v_cmp_gt_i32_e32 vcc, 15, v18
	s_and_saveexec_b64 s[4:5], vcc
	s_cbranch_execz .LBB3_36
	v_max_i32_e32 v9, 1, v44
	v_cvt_f32_u32_e32 v9, v9
	v_rcp_iflag_f32_e32 v44, v9
	s_nop 0
	v_pk_mul_f32 v[10:11], v[44:45], s[2:3]
	s_nop 0
	v_mul_f32_e32 v14, 0x4b800000, v10
	v_pk_mul_f32 v[16:17], v[10:11], v[10:11] op_sel:[0,1] op_sel_hi:[1,0]
	s_nop 0
	v_pk_fma_f32 v[10:11], v[42:43], v[14:15], v[16:17] op_sel_hi:[1,0,0]
	v_fma_mixlo_f16 v9, v56, v14, v16
	v_pk_fma_f32 v[12:13], v[36:37], v[14:15], v[16:17] op_sel_hi:[1,0,0]
	v_pk_fma_f32 v[30:31], v[30:31], v[14:15], v[16:17] op_sel_hi:[1,0,0]
	v_cvt_pk_f16_f32 v11, v10, v11
	v_cvt_pk_f16_f32 v12, v12, v13
	v_pack_b32_f16 v10, v9, v11
	v_cvt_pk_f16_f32 v9, v30, v31
	v_alignbit_b32 v11, v12, v11, 16
	v_alignbit_b32 v12, v9, v12, 16
	v_lshrrev_b32_e32 v13, 16, v9
	v_add_u32_e32 v9, v18, v75
	v_fma_mixhi_f16 v13, v49, v14, v16
	v_xor_b32_e32 v14, v9, v0
	v_lshlrev_b32_e32 v14, 4, v14
	v_and_b32_e32 v14, 0xf0, v14
	v_lshl_or_b32 v9, v9, 8, v14
	ds_write_b128 v9, v[10:13]

.LBB3_41:
	s_add_i32 s25, s25, 1
	global_load_dwordx2 v[38:39], v79, s[10:11]
	global_load_dwordx2 v[40:41], v80, s[10:11]
	global_load_dword v57, v87, s[12:13]
	global_load_dword v58, v88, s[12:13]
	global_load_dwordx2 v[32:33], v81, s[10:11]
	global_load_dwordx2 v[34:35], v86, s[10:11]
	global_load_dword v54, v89, s[12:13]
	global_load_dword v55, v90, s[12:13]
	s_cmp_lg_u32 s25, s19
	s_cbranch_scc1 .LBB3_47
	s_cmp_eq_u32 s7, 0
	s_cbranch_scc1 .LBB3_45
	s_add_i32 s25, s7, 1
	s_mov_b32 s7, 2
	s_cmp_eq_u32 s25, 2
	v_mov_b32_e32 v3, v6
	v_mov_b32_e32 v5, v47
	s_mov_b32 s19, s15
	s_cbranch_scc1 .LBB3_46
	s_cmp_eq_u32 s25, 3
	s_cselect_b64 vcc, -1, 0
	s_and_b64 s[26:27], vcc, exec
	v_cndmask_b32_e32 v5, 0, v48, vcc
	s_cselect_b32 s19, s6, 0x7fffffff
	s_mov_b32 s7, s25
	v_mov_b32_e32 v3, v7
	s_branch .LBB3_46

.LBB3_47:
	s_lshl_b32 s26, s25, 2
	v_add_u32_e32 v82, s26, v3
	v_lshl_add_u32 v82, v82, 2, v2
	ds_read_b32 v83, v82 offset:15360
	ds_read_b32 v84, v82 offset:15364
	ds_read_b32 v85, v82 offset:15368
	ds_read_b32 v82, v82 offset:15372
	v_cmp_lt_i32_e32 vcc, s26, v5
	s_or_b32 s28, s26, 1
	s_or_b32 s29, s26, 2
	s_waitcnt lgkmcnt(0)
	v_cndmask_b32_e32 v87, v8, v83, vcc
	v_cmp_lt_i32_e32 vcc, s28, v5
	s_or_b32 s30, s26, 3
	s_nop 0
	v_cndmask_b32_e32 v88, v8, v84, vcc
	v_cmp_lt_i32_e32 vcc, s29, v5
	v_lshl_or_b32 v79, v87, 7, v78
	v_lshlrev_b32_e32 v87, 2, v87
	v_cndmask_b32_e32 v89, v8, v85, vcc
	v_cmp_lt_i32_e32 vcc, s30, v5
	v_lshl_or_b32 v80, v88, 7, v78
	v_lshl_or_b32 v81, v89, 7, v78
	v_cndmask_b32_e32 v90, v8, v82, vcc
	v_lshl_or_b32 v86, v90, 7, v78
	v_lshlrev_b32_e32 v88, 2, v88
	v_lshlrev_b32_e32 v89, 2, v89
	v_lshlrev_b32_e32 v90, 2, v90
	s_waitcnt vmcnt(12)
	v_cvt_pk_f16_f32 v9, v52, v53
	v_perm_b32 v10, v28, v26, s21
	v_dot2c_f32_f16_e32 v56, v10, v9
	v_perm_b32 v10, v28, v26, s22
	v_dot2c_f32_f16_e32 v42, v10, v9
	v_perm_b32 v10, v28, v26, s23
	v_dot2c_f32_f16_e32 v43, v10, v9
	v_perm_b32 v10, v28, v26, s24
	v_dot2c_f32_f16_e32 v36, v10, v9
	v_perm_b32 v10, v29, v27, s21
	v_dot2c_f32_f16_e32 v37, v10, v9
	v_perm_b32 v10, v29, v27, s22
	v_dot2c_f32_f16_e32 v30, v10, v9
	v_perm_b32 v10, v29, v27, s23
	v_dot2c_f32_f16_e32 v31, v10, v9
	v_perm_b32 v10, v29, v27, s24
	v_dot2c_f32_f16_e32 v49, v10, v9
	s_waitcnt vmcnt(8)
	v_cvt_pk_f16_f32 v9, v50, v51
	v_perm_b32 v10, v24, v22, s21
	v_dot2c_f32_f16_e32 v56, v10, v9
	v_perm_b32 v10, v24, v22, s22
	v_dot2c_f32_f16_e32 v42, v10, v9
	v_perm_b32 v10, v24, v22, s23
	v_dot2c_f32_f16_e32 v43, v10, v9
	v_perm_b32 v10, v24, v22, s24
	v_dot2c_f32_f16_e32 v36, v10, v9
	v_perm_b32 v10, v25, v23, s21
	v_dot2c_f32_f16_e32 v37, v10, v9
	v_perm_b32 v10, v25, v23, s22
	v_dot2c_f32_f16_e32 v30, v10, v9
	v_perm_b32 v10, v25, v23, s23
	v_dot2c_f32_f16_e32 v31, v10, v9
	v_perm_b32 v10, v25, v23, s24
	s_add_i32 s5, s5, 1
	v_dot2c_f32_f16_e32 v49, v10, v9
	s_cmp_lg_u32 s5, s4
	s_cbranch_scc1 .LBB3_55
	v_cmp_gt_i32_e32 vcc, 15, v18
	s_and_saveexec_b64 s[4:5], vcc
	s_cbranch_execz .LBB3_50
	v_max_i32_e32 v9, 1, v44
	v_cvt_f32_u32_e32 v9, v9
	v_rcp_iflag_f32_e32 v44, v9
	s_nop 0
	v_pk_mul_f32 v[10:11], v[44:45], s[2:3]
	s_nop 0
	v_mul_f32_e32 v14, 0x4b800000, v10
	v_pk_mul_f32 v[16:17], v[10:11], v[10:11] op_sel:[0,1] op_sel_hi:[1,0]
	s_nop 0
	v_pk_fma_f32 v[10:11], v[42:43], v[14:15], v[16:17] op_sel_hi:[1,0,0]
	v_fma_mixlo_f16 v9, v56, v14, v16
	v_pk_fma_f32 v[12:13], v[36:37], v[14:15], v[16:17] op_sel_hi:[1,0,0]
	v_pk_fma_f32 v[22:23], v[30:31], v[14:15], v[16:17] op_sel_hi:[1,0,0]
	v_cvt_pk_f16_f32 v11, v10, v11
	v_cvt_pk_f16_f32 v12, v12, v13
	v_pack_b32_f16 v10, v9, v11
	v_cvt_pk_f16_f32 v9, v22, v23
	v_alignbit_b32 v11, v12, v11, 16
	v_alignbit_b32 v12, v9, v12, 16
	v_lshrrev_b32_e32 v13, 16, v9
	v_add_u32_e32 v9, v18, v75
	v_fma_mixhi_f16 v13, v49, v14, v16
	v_xor_b32_e32 v14, v9, v0
	v_lshlrev_b32_e32 v14, 4, v14
	v_and_b32_e32 v14, 0xf0, v14
	v_lshl_or_b32 v9, v9, 8, v14
	ds_write_b128 v9, v[10:13]

.LBB3_55:
	s_add_i32 s25, s25, 1
	global_load_dwordx2 v[26:27], v79, s[10:11]
	global_load_dwordx2 v[28:29], v80, s[10:11]
	global_load_dword v52, v87, s[12:13]
	global_load_dword v53, v88, s[12:13]
	global_load_dwordx2 v[22:23], v81, s[10:11]
	global_load_dwordx2 v[24:25], v86, s[10:11]
	global_load_dword v50, v89, s[12:13]
	global_load_dword v51, v90, s[12:13]
	s_cmp_lg_u32 s25, s19
	s_cbranch_scc1 .LBB3_32
	s_cmp_eq_u32 s7, 0
	s_cbranch_scc1 .LBB3_30
	s_add_i32 s25, s7, 1
	s_mov_b32 s7, 2
	s_cmp_eq_u32 s25, 2
	v_mov_b32_e32 v3, v6
	v_mov_b32_e32 v5, v47
	s_mov_b32 s19, s15
	s_cbranch_scc1 .LBB3_31
	s_cmp_eq_u32 s25, 3
	s_cselect_b64 vcc, -1, 0
	s_and_b64 s[26:27], vcc, exec
	v_cndmask_b32_e32 v5, 0, v48, vcc
	s_cselect_b32 s19, s6, 0x7fffffff
	s_mov_b32 s7, s25
	v_mov_b32_e32 v3, v7
	s_branch .LBB3_31
